# speedup vs baseline: 1.0176x; 1.0176x over previous
.LBB6_9:
	v_add_u32_e32 v138, s27, v207
	ds_read_b64_tr_b16 v[156:157], v138 offset:24576
	ds_read_b64_tr_b16 v[158:159], v138 offset:25088
	v_add_f32_e32 v120, v80, v81
	s_waitcnt lgkmcnt(2)
	v_mfma_scale_f32_32x32x64_f8f6f4 v[48:63], v[112:119], v[96:103], v[48:63], v219, v220 op_sel_hi:[0,0,0]
	v_add_f32_e32 v112, v82, v120
	v_add_f32_e32 v112, v83, v112
	v_add_f32_e32 v112, v84, v112
	v_add_f32_e32 v116, v85, v112
	v_cvt_pk_f16_f32 v132, v80, v81
	v_cvt_pk_f16_f32 v133, v82, v83
	ds_read_b64_tr_b16 v[112:113], v138 offset:28672
	ds_read_b64_tr_b16 v[114:115], v138 offset:29184
	v_add_f32_e32 v80, v86, v116
	v_add_f32_e32 v80, v87, v80
	v_add_f32_e32 v80, v88, v80
	v_add_f32_e32 v80, v89, v80
	v_cvt_pk_f16_f32 v134, v84, v85
	v_cvt_pk_f16_f32 v135, v86, v87
	s_waitcnt lgkmcnt(4)
	v_mfma_scale_f32_32x32x64_f8f6f4 v[32:47], v[104:111], v[96:103], v[32:47], v219, v220 op_sel_hi:[0,0,0]
	ds_read_b64_tr_b16 v[104:105], v138 offset:25600
	ds_read_b64_tr_b16 v[106:107], v138 offset:26112
	v_add_f32_e32 v80, v90, v80
	v_add_f32_e32 v80, v91, v80
	v_add_f32_e32 v80, v92, v80
	v_add_f32_e32 v80, v93, v80
	v_cvt_pk_f16_f32 v128, v88, v89
	v_cvt_pk_f16_f32 v129, v90, v91
	ds_read_b64_tr_b16 v[152:153], v138 offset:29696
	ds_read_b64_tr_b16 v[154:155], v138 offset:30208
	v_add_f32_e32 v80, v94, v80
	v_add_f32_e32 v80, v95, v80
	v_add_f32_e32 v80, v64, v80
	v_add_f32_e32 v80, v65, v80
	v_cvt_pk_f16_f32 v130, v92, v93
	v_cvt_pk_f16_f32 v131, v94, v95
	ds_read_b64_tr_b16 v[148:149], v138 offset:26624
	ds_read_b64_tr_b16 v[150:151], v138 offset:27136
	v_add_f32_e32 v80, v66, v80
	v_add_f32_e32 v80, v67, v80
	v_add_f32_e32 v80, v68, v80
	v_add_f32_e32 v80, v69, v80
	v_cvt_pk_f16_f32 v124, v64, v65
	v_cvt_pk_f16_f32 v125, v66, v67
	ds_read_b64_tr_b16 v[144:145], v138 offset:30720
	ds_read_b64_tr_b16 v[146:147], v138 offset:31232
	v_add_f32_e32 v64, v70, v80
	v_add_f32_e32 v64, v71, v64
	v_add_f32_e32 v64, v72, v64
	v_add_f32_e32 v64, v73, v64
	v_cvt_pk_f16_f32 v126, v68, v69
	v_cvt_pk_f16_f32 v127, v70, v71
	ds_read_b64_tr_b16 v[140:141], v138 offset:27648
	ds_read_b64_tr_b16 v[142:143], v138 offset:28160
	v_add_f32_e32 v64, v74, v64
	v_add_f32_e32 v64, v75, v64
	v_add_f32_e32 v64, v76, v64
	v_add_f32_e32 v64, v77, v64
	v_cvt_pk_f16_f32 v120, v72, v73
	v_cvt_pk_f16_f32 v121, v74, v75
	ds_read_b64_tr_b16 v[136:137], v138 offset:31744
	ds_read_b64_tr_b16 v[138:139], v138 offset:32256
	v_add_f32_e32 v64, v78, v64
	v_add_f32_e32 v64, v79, v64
	v_add_f32_e32 v108, 0, v64
	v_cvt_pk_f16_f32 v122, v76, v77
	v_cvt_pk_f16_f32 v123, v78, v79
	s_nop 1
	s_nop 0
	v_add_f32_e32 v185, v185, v108
	v_max_f32_e32 v108, v49, v49
	v_max_f32_e32 v109, v48, v48
	v_max_f32_e32 v108, v109, v108
	v_max3_f32 v109, v50, v51, v33
	v_max3_f32 v108, v108, v32, v34
	v_max3_f32 v108, v108, v35, v52
	v_max3_f32 v109, v109, v54, v55
	v_max3_f32 v108, v108, v53, v36
	v_max3_f32 v109, v109, v38, v39
	v_max3_f32 v108, v108, v37, v56
	v_max3_f32 v109, v109, v58, v59
	v_add_u32_e32 v221, v222, v223
	v_max3_f32 v108, v108, v57, v40
	v_max3_f32 v109, v109, v42, v43
	v_max3_f32 v108, v108, v41, v60
	v_max3_f32 v109, v109, v62, v63
	v_max3_f32 v108, v108, v61, v44
	v_max3_f32 v109, v109, v46, v47
	v_max3_f32 v108, v108, v45, v109
	v_mov_b32_e32 v109, v108
	s_nop 1
	v_permlane32_swap_b32_e32 v108, v109
	v_max_f32_e32 v109, v109, v109
	v_max_f32_e32 v108, v108, v108
	v_max_f32_e32 v108, v108, v109
	v_fma_f32 v108, v108, s41, -v208
	v_cmp_lt_f32_e32 vcc, s29, v108
	s_cmp_lg_u64 vcc, 0
	s_cselect_b64 s[24:25], -1, 0
	s_cbranch_vccnz .LBB6_21

.LBB6_12:
	v_mfma_f32_32x32x16_f16 v[16:31], v[132:135], v[112:115], v[16:31]
	v_fma_f32 v52, v52, s41, -v208
	v_fma_f32 v53, v53, s41, -v208
	v_fma_f32 v54, v54, s41, -v208
	v_fma_f32 v55, v55, s41, -v208
	v_exp_f32_e32 v52, v52
	v_exp_f32_e32 v53, v53
	v_exp_f32_e32 v54, v54
	v_exp_f32_e32 v55, v55
	v_lshl_add_u64 v[108:109], v[182:183], 0, s[20:21]
	s_add_i32 s26, s28, s37
	s_mov_b32 m0, s26
	s_nop 0
	global_load_lds_dwordx4 v[108:109], off
	v_lshl_add_u64 v[226:227], v[108:109], 0, s[58:59]
	s_add_i32 m0, s26, 0x6800
	s_nop 0
	global_load_lds_dwordx4 v[226:227], off
	s_waitcnt lgkmcnt(0)
	v_lshl_add_u64 v[186:187], v[164:165], 0, s[2:3]
	v_lshl_add_u64 v[108:109], v[186:187], 0, s[10:11]
	v_lshl_add_u64 v[108:109], v[108:109], 0, s[62:63]
	s_add_i32 m0, s38, s65
	s_nop 0
	global_load_lds_dwordx4 v[108:109], off nt
	v_add_u32_e32 v108, s28, v216
	v_add_u32_e32 v109, v108, v217
	v_add_u32_e32 v108, v108, v218
	ds_read_b128 v[112:115], v109
	ds_read_b128 v[116:119], v108
	v_mfma_f32_32x32x16_f16 v[0:15], v[128:131], v[104:107], v[0:15]
	v_fma_f32 v56, v56, s41, -v208
	v_fma_f32 v57, v57, s41, -v208
	v_fma_f32 v58, v58, s41, -v208
	v_fma_f32 v59, v59, s41, -v208
	v_exp_f32_e32 v56, v56
	v_exp_f32_e32 v57, v57
	v_exp_f32_e32 v58, v58
	v_exp_f32_e32 v59, v59
	v_lshl_add_u64 v[188:189], v[178:179], 0, s[2:3]
	v_lshl_add_u64 v[104:105], v[188:189], 0, s[10:11]
	v_lshl_add_u64 v[104:105], v[104:105], 0, s[62:63]
	s_add_i32 m0, s30, s65
	s_nop 0
	global_load_lds_dwordx4 v[104:105], off nt
	ds_read_b128 v[104:107], v109 offset:2048
	ds_read_b128 v[108:111], v108 offset:2048
	v_mfma_f32_32x32x16_f16 v[16:31], v[128:131], v[152:155], v[16:31]
	v_fma_f32 v60, v60, s41, -v208
	v_fma_f32 v61, v61, s41, -v208
	v_fma_f32 v62, v62, s41, -v208
	v_fma_f32 v63, v63, s41, -v208
	v_exp_f32_e32 v60, v60
	v_exp_f32_e32 v61, v61
	v_exp_f32_e32 v62, v62
	v_exp_f32_e32 v63, v63
	v_lshl_add_u64 v[190:191], v[176:177], 0, s[2:3]
	v_lshl_add_u64 v[128:129], v[190:191], 0, s[10:11]
	v_lshl_add_u64 v[128:129], v[128:129], 0, s[62:63]
	s_add_i32 m0, s31, s65
	s_nop 0
	global_load_lds_dwordx4 v[128:129], off nt
	v_mfma_f32_32x32x16_f16 v[0:15], v[124:127], v[148:151], v[0:15]
	v_fma_f32 v32, v32, s41, -v208
	v_fma_f32 v33, v33, s41, -v208
	v_fma_f32 v34, v34, s41, -v208
	v_fma_f32 v35, v35, s41, -v208
	v_exp_f32_e32 v32, v32
	v_exp_f32_e32 v33, v33
	v_exp_f32_e32 v34, v34
	v_exp_f32_e32 v35, v35
	v_lshl_add_u64 v[192:193], v[174:175], 0, s[2:3]
	v_lshl_add_u64 v[128:129], v[192:193], 0, s[10:11]
	v_lshl_add_u64 v[128:129], v[128:129], 0, s[62:63]
	s_add_i32 m0, s34, s65
	s_nop 0
	global_load_lds_dwordx4 v[128:129], off nt
	s_waitcnt lgkmcnt(14)
	v_mfma_f32_32x32x16_f16 v[16:31], v[124:127], v[144:147], v[16:31]
	v_fma_f32 v36, v36, s41, -v208
	v_fma_f32 v37, v37, s41, -v208
	v_fma_f32 v38, v38, s41, -v208
	v_fma_f32 v39, v39, s41, -v208
	v_exp_f32_e32 v36, v36
	v_exp_f32_e32 v37, v37
	v_exp_f32_e32 v38, v38
	v_exp_f32_e32 v39, v39
	v_lshl_add_u64 v[194:195], v[172:173], 0, s[2:3]
	v_mfma_f32_32x32x16_f16 v[0:15], v[120:123], v[140:143], v[0:15]
	v_fma_f32 v40, v40, s41, -v208
	v_fma_f32 v41, v41, s41, -v208
	v_fma_f32 v42, v42, s41, -v208
	v_fma_f32 v43, v43, s41, -v208
	v_exp_f32_e32 v40, v40
	v_exp_f32_e32 v41, v41
	v_exp_f32_e32 v42, v42
	v_exp_f32_e32 v43, v43
	v_lshl_add_u64 v[196:197], v[170:171], 0, s[2:3]
	s_waitcnt lgkmcnt(12)
	v_mfma_f32_32x32x16_f16 v[16:31], v[120:123], v[136:139], v[16:31]
	v_fma_f32 v44, v44, s41, -v208
	v_fma_f32 v45, v45, s41, -v208
	v_fma_f32 v46, v46, s41, -v208
	v_fma_f32 v47, v47, s41, -v208
	v_exp_f32_e32 v44, v44
	v_exp_f32_e32 v45, v45
	v_exp_f32_e32 v46, v46
	v_exp_f32_e32 v47, v47
	v_lshl_add_u64 v[198:199], v[168:169], 0, s[2:3]
	v_lshl_add_u64 v[200:201], v[166:167], 0, s[2:3]
	s_waitcnt vmcnt(7) lgkmcnt(0)
	s_barrier
	ds_read_b128 v[80:83], v221
	ds_read_b128 v[64:67], v161
	ds_read_b128 v[84:87], v184
	ds_read_b128 v[68:71], v211
	ds_read_b128 v[88:91], v212
	ds_read_b128 v[72:75], v213
	ds_read_b128 v[92:95], v214
	ds_read_b128 v[76:79], v215
	s_andn2_b64 vcc, exec, s[24:25]
	s_cbranch_vccnz .LBB6_14
	ds_read_b128 v[136:139], v205 offset:49248
	ds_read_b128 v[140:143], v205 offset:49216
	ds_read_b128 v[144:147], v205 offset:49184
	ds_read_b128 v[148:151], v205 offset:49152
	s_waitcnt lgkmcnt(3)
	v_pk_mul_f32 v[14:15], v[14:15], v[138:139]
	s_waitcnt lgkmcnt(2)
	v_pk_mul_f32 v[10:11], v[10:11], v[142:143]
	s_waitcnt lgkmcnt(1)
	v_pk_mul_f32 v[6:7], v[6:7], v[146:147]
	s_waitcnt lgkmcnt(0)
	v_pk_mul_f32 v[2:3], v[2:3], v[150:151]
	v_pk_mul_f32 v[12:13], v[12:13], v[136:137]
	v_pk_mul_f32 v[8:9], v[8:9], v[140:141]
	v_pk_mul_f32 v[4:5], v[4:5], v[144:145]
	v_pk_mul_f32 v[0:1], v[0:1], v[148:149]
	v_pk_mul_f32 v[30:31], v[30:31], v[138:139]
	v_pk_mul_f32 v[26:27], v[26:27], v[142:143]
	v_pk_mul_f32 v[22:23], v[22:23], v[146:147]
	v_pk_mul_f32 v[18:19], v[18:19], v[150:151]
	v_pk_mul_f32 v[28:29], v[28:29], v[136:137]
	v_pk_mul_f32 v[24:25], v[24:25], v[140:141]
	v_pk_mul_f32 v[20:21], v[20:21], v[144:145]
	v_pk_mul_f32 v[16:17], v[16:17], v[148:149]
.LBB6_14:
	v_add_u32_e32 v138, s45, v207
	ds_read_b64_tr_b16 v[156:157], v138 offset:24576
	ds_read_b64_tr_b16 v[158:159], v138 offset:25088
	v_add_f32_e32 v120, v48, v49
	s_waitcnt lgkmcnt(2)
	v_mfma_scale_f32_32x32x64_f8f6f4 v[80:95], v[112:119], v[96:103], v[80:95], v219, v220 op_sel_hi:[0,0,0]
	v_add_f32_e32 v112, v50, v120
	v_add_f32_e32 v112, v51, v112
	v_add_f32_e32 v112, v52, v112
	v_add_f32_e32 v116, v53, v112
	v_cvt_pk_f16_f32 v132, v48, v49
	v_cvt_pk_f16_f32 v133, v50, v51
	ds_read_b64_tr_b16 v[112:113], v138 offset:28672
	ds_read_b64_tr_b16 v[114:115], v138 offset:29184
	v_add_f32_e32 v48, v54, v116
	v_add_f32_e32 v48, v55, v48
	v_add_f32_e32 v48, v56, v48
	v_add_f32_e32 v48, v57, v48
	v_cvt_pk_f16_f32 v134, v52, v53
	v_cvt_pk_f16_f32 v135, v54, v55
	s_waitcnt lgkmcnt(4)
	v_mfma_scale_f32_32x32x64_f8f6f4 v[64:79], v[104:111], v[96:103], v[64:79], v219, v220 op_sel_hi:[0,0,0]
	ds_read_b64_tr_b16 v[104:105], v138 offset:25600
	ds_read_b64_tr_b16 v[106:107], v138 offset:26112
	v_add_f32_e32 v48, v58, v48
	v_add_f32_e32 v48, v59, v48
	v_add_f32_e32 v48, v60, v48
	v_add_f32_e32 v48, v61, v48
	v_cvt_pk_f16_f32 v128, v56, v57
	v_cvt_pk_f16_f32 v129, v58, v59
	ds_read_b64_tr_b16 v[152:153], v138 offset:29696
	ds_read_b64_tr_b16 v[154:155], v138 offset:30208
	v_add_f32_e32 v48, v62, v48
	v_add_f32_e32 v48, v63, v48
	v_add_f32_e32 v48, v32, v48
	v_add_f32_e32 v48, v33, v48
	v_cvt_pk_f16_f32 v130, v60, v61
	v_cvt_pk_f16_f32 v131, v62, v63
	ds_read_b64_tr_b16 v[148:149], v138 offset:26624
	ds_read_b64_tr_b16 v[150:151], v138 offset:27136
	v_add_f32_e32 v48, v34, v48
	v_add_f32_e32 v48, v35, v48
	v_add_f32_e32 v48, v36, v48
	v_add_f32_e32 v48, v37, v48
	v_cvt_pk_f16_f32 v124, v32, v33
	v_cvt_pk_f16_f32 v125, v34, v35
	ds_read_b64_tr_b16 v[144:145], v138 offset:30720
	ds_read_b64_tr_b16 v[146:147], v138 offset:31232
	v_add_f32_e32 v32, v38, v48
	v_add_f32_e32 v32, v39, v32
	v_add_f32_e32 v32, v40, v32
	v_add_f32_e32 v32, v41, v32
	v_cvt_pk_f16_f32 v126, v36, v37
	v_cvt_pk_f16_f32 v127, v38, v39
	ds_read_b64_tr_b16 v[140:141], v138 offset:27648
	ds_read_b64_tr_b16 v[142:143], v138 offset:28160
	v_add_f32_e32 v32, v42, v32
	v_add_f32_e32 v32, v43, v32
	v_add_f32_e32 v32, v44, v32
	v_add_f32_e32 v32, v45, v32
	v_cvt_pk_f16_f32 v120, v40, v41
	v_cvt_pk_f16_f32 v121, v42, v43
	ds_read_b64_tr_b16 v[136:137], v138 offset:31744
	ds_read_b64_tr_b16 v[138:139], v138 offset:32256
	v_add_f32_e32 v32, v46, v32
	v_add_f32_e32 v32, v47, v32
	v_add_f32_e32 v108, 0, v32
	v_cvt_pk_f16_f32 v122, v44, v45
	v_cvt_pk_f16_f32 v123, v46, v47
	s_nop 1
	s_nop 0
	v_add_f32_e32 v185, v185, v108
	v_max_f32_e32 v108, v81, v81
	v_max_f32_e32 v109, v80, v80
	v_max_f32_e32 v108, v109, v108
	v_max3_f32 v109, v82, v83, v65
	v_max3_f32 v108, v108, v64, v66
	v_max3_f32 v108, v108, v67, v84
	v_max3_f32 v109, v109, v86, v87
	v_max3_f32 v108, v108, v85, v68
	v_max3_f32 v109, v109, v70, v71
	v_max3_f32 v108, v108, v69, v88
	v_max3_f32 v109, v109, v90, v91
	v_max3_f32 v108, v108, v89, v72
	v_max3_f32 v109, v109, v74, v75
	v_max3_f32 v108, v108, v73, v92
	v_max3_f32 v109, v109, v94, v95
	v_max3_f32 v108, v108, v93, v76
	v_max3_f32 v109, v109, v78, v79
	v_max3_f32 v108, v108, v77, v109
	v_mov_b32_e32 v109, v108
	s_nop 1
	v_permlane32_swap_b32_e32 v108, v109
	v_max_f32_e32 v109, v109, v109
	v_max_f32_e32 v108, v108, v108
	v_max_f32_e32 v108, v108, v109
	v_fma_f32 v108, v108, s41, -v208
	v_cmp_lt_f32_e32 vcc, s29, v108
	s_cmp_lg_u64 vcc, 0
	s_cselect_b64 s[24:25], -1, 0
	s_cbranch_vccnz .LBB6_24

.LBB6_17:
	s_add_i32 s26, s28, 0x2000
	s_cmpk_lg_i32 s28, 0x4000
	s_cselect_b32 s45, s26, 0
	v_mfma_f32_32x32x16_f16 v[16:31], v[132:135], v[112:115], v[16:31]
	v_fma_f32 v84, v84, s41, -v208
	v_fma_f32 v85, v85, s41, -v208
	v_fma_f32 v86, v86, s41, -v208
	v_fma_f32 v87, v87, s41, -v208
	v_exp_f32_e32 v84, v84
	v_exp_f32_e32 v85, v85
	v_exp_f32_e32 v86, v86
	v_exp_f32_e32 v87, v87
	v_lshl_add_u64 v[182:183], v[182:183], 0, s[12:13]
	s_add_i32 s26, s45, s37
	s_mov_b32 m0, s26
	s_nop 0
	global_load_lds_dwordx4 v[182:183], off
	v_lshl_add_u64 v[226:227], v[182:183], 0, s[58:59]
	s_add_i32 m0, s26, 0x6800
	s_nop 0
	global_load_lds_dwordx4 v[226:227], off
	s_waitcnt lgkmcnt(0)
	v_lshl_add_u64 v[108:109], v[186:187], 0, s[22:23]
	v_lshl_add_u64 v[108:109], v[108:109], 0, s[62:63]
	s_add_i32 m0, s38, s64
	s_nop 0
	global_load_lds_dwordx4 v[108:109], off nt
	v_add_u32_e32 v108, s45, v216
	v_add_u32_e32 v109, v108, v217
	v_add_u32_e32 v108, v108, v218
	ds_read_b128 v[112:115], v109
	ds_read_b128 v[116:119], v108
	v_mfma_f32_32x32x16_f16 v[0:15], v[128:131], v[104:107], v[0:15]
	v_fma_f32 v88, v88, s41, -v208
	v_fma_f32 v89, v89, s41, -v208
	v_fma_f32 v90, v90, s41, -v208
	v_fma_f32 v91, v91, s41, -v208
	v_exp_f32_e32 v88, v88
	v_exp_f32_e32 v89, v89
	v_exp_f32_e32 v90, v90
	v_exp_f32_e32 v91, v91
	v_lshl_add_u64 v[104:105], v[188:189], 0, s[22:23]
	v_lshl_add_u64 v[104:105], v[104:105], 0, s[62:63]
	s_add_i32 m0, s30, s64
	s_nop 0
	global_load_lds_dwordx4 v[104:105], off nt
	ds_read_b128 v[104:107], v109 offset:2048
	ds_read_b128 v[108:111], v108 offset:2048
	v_mfma_f32_32x32x16_f16 v[16:31], v[128:131], v[152:155], v[16:31]
	v_fma_f32 v92, v92, s41, -v208
	v_fma_f32 v93, v93, s41, -v208
	v_fma_f32 v94, v94, s41, -v208
	v_fma_f32 v95, v95, s41, -v208
	v_exp_f32_e32 v92, v92
	v_exp_f32_e32 v93, v93
	v_exp_f32_e32 v94, v94
	v_exp_f32_e32 v95, v95
	v_lshl_add_u64 v[128:129], v[190:191], 0, s[22:23]
	v_lshl_add_u64 v[128:129], v[128:129], 0, s[62:63]
	s_add_i32 m0, s31, s64
	s_nop 0
	global_load_lds_dwordx4 v[128:129], off nt
	v_mfma_f32_32x32x16_f16 v[0:15], v[124:127], v[148:151], v[0:15]
	v_fma_f32 v64, v64, s41, -v208
	v_fma_f32 v65, v65, s41, -v208
	v_fma_f32 v66, v66, s41, -v208
	v_fma_f32 v67, v67, s41, -v208
	v_exp_f32_e32 v64, v64
	v_exp_f32_e32 v65, v65
	v_exp_f32_e32 v66, v66
	v_exp_f32_e32 v67, v67
	v_lshl_add_u64 v[128:129], v[192:193], 0, s[22:23]
	v_lshl_add_u64 v[128:129], v[128:129], 0, s[62:63]
	s_add_i32 m0, s34, s64
	s_nop 0
	global_load_lds_dwordx4 v[128:129], off nt
	s_waitcnt lgkmcnt(14)
	v_mfma_f32_32x32x16_f16 v[16:31], v[124:127], v[144:147], v[16:31]
	v_fma_f32 v68, v68, s41, -v208
	v_fma_f32 v69, v69, s41, -v208
	v_fma_f32 v70, v70, s41, -v208
	v_fma_f32 v71, v71, s41, -v208
	v_exp_f32_e32 v68, v68
	v_exp_f32_e32 v69, v69
	v_exp_f32_e32 v70, v70
	v_exp_f32_e32 v71, v71
	v_mfma_f32_32x32x16_f16 v[0:15], v[120:123], v[140:143], v[0:15]
	v_fma_f32 v72, v72, s41, -v208
	v_fma_f32 v73, v73, s41, -v208
	v_fma_f32 v74, v74, s41, -v208
	v_fma_f32 v75, v75, s41, -v208
	v_exp_f32_e32 v72, v72
	v_exp_f32_e32 v73, v73
	v_exp_f32_e32 v74, v74
	v_exp_f32_e32 v75, v75
	s_waitcnt lgkmcnt(12)
	v_mfma_f32_32x32x16_f16 v[16:31], v[120:123], v[136:139], v[16:31]
	v_fma_f32 v76, v76, s41, -v208
	v_fma_f32 v77, v77, s41, -v208
	v_fma_f32 v78, v78, s41, -v208
	v_fma_f32 v79, v79, s41, -v208
	v_exp_f32_e32 v76, v76
	v_exp_f32_e32 v77, v77
	v_exp_f32_e32 v78, v78
	v_exp_f32_e32 v79, v79
	s_waitcnt vmcnt(7) lgkmcnt(0)
	s_barrier
	ds_read_b128 v[48:51], v221 offset:32768
	ds_read_b128 v[32:35], v161 offset:32768
	ds_read_b128 v[52:55], v184 offset:32768
	ds_read_b128 v[36:39], v211 offset:32768
	ds_read_b128 v[56:59], v212 offset:32768
	ds_read_b128 v[40:43], v213 offset:32768
	ds_read_b128 v[60:63], v214 offset:32768
	ds_read_b128 v[44:47], v215 offset:32768
	s_andn2_b64 vcc, exec, s[24:25]
	s_cbranch_vccnz .LBB6_19
	ds_read_b128 v[136:139], v205 offset:49248
	ds_read_b128 v[140:143], v205 offset:49216
	ds_read_b128 v[144:147], v205 offset:49184
	ds_read_b128 v[148:151], v205 offset:49152
	s_waitcnt lgkmcnt(3)
	v_pk_mul_f32 v[14:15], v[14:15], v[138:139]
	s_waitcnt lgkmcnt(2)
	v_pk_mul_f32 v[10:11], v[10:11], v[142:143]
	s_waitcnt lgkmcnt(1)
	v_pk_mul_f32 v[6:7], v[6:7], v[146:147]
	s_waitcnt lgkmcnt(0)
	v_pk_mul_f32 v[2:3], v[2:3], v[150:151]
	v_pk_mul_f32 v[12:13], v[12:13], v[136:137]
	v_pk_mul_f32 v[8:9], v[8:9], v[140:141]
	v_pk_mul_f32 v[4:5], v[4:5], v[144:145]
	v_pk_mul_f32 v[0:1], v[0:1], v[148:149]
	v_pk_mul_f32 v[30:31], v[30:31], v[138:139]
	v_pk_mul_f32 v[26:27], v[26:27], v[142:143]
	v_pk_mul_f32 v[22:23], v[22:23], v[146:147]
	v_pk_mul_f32 v[18:19], v[18:19], v[150:151]
	v_pk_mul_f32 v[28:29], v[28:29], v[136:137]
	v_pk_mul_f32 v[24:25], v[24:25], v[140:141]
	v_pk_mul_f32 v[20:21], v[20:21], v[144:145]
	v_pk_mul_f32 v[16:17], v[16:17], v[148:149]

.LBB6_27:
	ds_read_b64_tr_b16 v[156:157], v207 offset:32768
	ds_read_b64_tr_b16 v[158:159], v207 offset:33280
	v_add_f32_e32 v120, v80, v81
	v_mov_b32_e32 v121, 0x7f7f7f7f
	v_mov_b32_e32 v124, 0x7c7c7c7c
	s_waitcnt lgkmcnt(2)
	v_mfma_scale_f32_32x32x64_f8f6f4 v[48:63], v[112:119], v[96:103], v[48:63], v121, v124 op_sel_hi:[0,0,0]
	v_add_f32_e32 v112, v82, v120
	v_add_f32_e32 v112, v83, v112
	v_add_f32_e32 v112, v84, v112
	v_add_f32_e32 v116, v85, v112
	v_cvt_pk_f16_f32 v132, v80, v81
	v_cvt_pk_f16_f32 v133, v82, v83
	ds_read_b64_tr_b16 v[112:113], v207 offset:36864
	ds_read_b64_tr_b16 v[114:115], v207 offset:37376
	v_add_f32_e32 v80, v86, v116
	v_add_f32_e32 v80, v87, v80
	v_add_f32_e32 v80, v88, v80
	v_add_f32_e32 v80, v89, v80
	v_cvt_pk_f16_f32 v134, v84, v85
	v_cvt_pk_f16_f32 v135, v86, v87
	s_waitcnt lgkmcnt(4)
	v_mfma_scale_f32_32x32x64_f8f6f4 v[32:47], v[104:111], v[96:103], v[32:47], v121, v124 op_sel_hi:[0,0,0]
	ds_read_b64_tr_b16 v[104:105], v207 offset:33792
	ds_read_b64_tr_b16 v[106:107], v207 offset:34304
	v_add_f32_e32 v80, v90, v80
	v_add_f32_e32 v80, v91, v80
	v_add_f32_e32 v80, v92, v80
	v_add_f32_e32 v80, v93, v80
	v_cvt_pk_f16_f32 v128, v88, v89
	v_cvt_pk_f16_f32 v129, v90, v91
	ds_read_b64_tr_b16 v[152:153], v207 offset:37888
	ds_read_b64_tr_b16 v[154:155], v207 offset:38400
	v_add_f32_e32 v80, v94, v80
	v_add_f32_e32 v80, v95, v80
	v_add_f32_e32 v80, v64, v80
	v_add_f32_e32 v80, v65, v80
	v_cvt_pk_f16_f32 v130, v92, v93
	v_cvt_pk_f16_f32 v131, v94, v95
	ds_read_b64_tr_b16 v[148:149], v207 offset:34816
	ds_read_b64_tr_b16 v[150:151], v207 offset:35328
	v_add_f32_e32 v80, v66, v80
	v_add_f32_e32 v80, v67, v80
	v_add_f32_e32 v80, v68, v80
	v_add_f32_e32 v80, v69, v80
	v_cvt_pk_f16_f32 v124, v64, v65
	v_cvt_pk_f16_f32 v125, v66, v67
	ds_read_b64_tr_b16 v[144:145], v207 offset:38912
	ds_read_b64_tr_b16 v[146:147], v207 offset:39424
	v_add_f32_e32 v64, v70, v80
	v_add_f32_e32 v64, v71, v64
	v_add_f32_e32 v64, v72, v64
	v_add_f32_e32 v64, v73, v64
	v_cvt_pk_f16_f32 v126, v68, v69
	v_cvt_pk_f16_f32 v127, v70, v71
	ds_read_b64_tr_b16 v[140:141], v207 offset:35840
	ds_read_b64_tr_b16 v[142:143], v207 offset:36352
	v_add_f32_e32 v64, v74, v64
	v_add_f32_e32 v64, v75, v64
	v_add_f32_e32 v64, v76, v64
	v_add_f32_e32 v64, v77, v64
	v_cvt_pk_f16_f32 v120, v72, v73
	v_cvt_pk_f16_f32 v121, v74, v75
	ds_read_b64_tr_b16 v[136:137], v207 offset:39936
	ds_read_b64_tr_b16 v[138:139], v207 offset:40448
	v_add_f32_e32 v64, v78, v64
	v_add_f32_e32 v64, v79, v64
	v_add_f32_e32 v108, 0, v64
	v_cvt_pk_f16_f32 v122, v76, v77
	v_cvt_pk_f16_f32 v123, v78, v79
	s_nop 1
	s_nop 0
	v_add_f32_e32 v180, v185, v108
	v_max_f32_e32 v108, v49, v49
	v_max_f32_e32 v109, v48, v48
	v_max_f32_e32 v108, v109, v108
	v_max3_f32 v109, v50, v51, v33
	v_max3_f32 v108, v108, v32, v34
	v_max3_f32 v108, v108, v35, v52
	v_max3_f32 v109, v109, v54, v55
	v_max3_f32 v108, v108, v53, v36
	v_max3_f32 v109, v109, v38, v39
	v_max3_f32 v108, v108, v37, v56
	v_max3_f32 v109, v109, v58, v59
	v_max3_f32 v108, v108, v57, v40
	v_max3_f32 v109, v109, v42, v43
	v_max3_f32 v108, v108, v41, v60
	v_max3_f32 v109, v109, v62, v63
	v_max3_f32 v108, v108, v61, v44
	v_max3_f32 v109, v109, v46, v47
	v_max3_f32 v108, v108, v45, v109
	v_mov_b32_e32 v109, v108
	s_nop 1
	v_permlane32_swap_b32_e32 v108, v109
	v_max_f32_e32 v109, v109, v109
	v_max_f32_e32 v108, v108, v108
	v_max_f32_e32 v108, v108, v109
	s_mov_b32 s8, 0x3fb8aa3b
	v_fma_f32 v108, v108, s8, -v208
	s_mov_b32 s2, 0x41000000
	v_cmp_lt_f32_e32 vcc, s2, v108
	s_cmp_lg_u64 vcc, 0
	s_cselect_b64 s[2:3], -1, 0
	s_cbranch_vccnz .LBB6_39
.LBB6_28:
	s_waitcnt lgkmcnt(14)
	v_mfma_f32_32x32x16_f16 v[0:15], v[132:135], v[156:159], v[0:15]
	v_fma_f32 v48, v48, s8, -v208
	v_fma_f32 v49, v49, s8, -v208
	v_fma_f32 v50, v50, s8, -v208
	v_fma_f32 v51, v51, s8, -v208
	v_exp_f32_e32 v48, v48
	v_exp_f32_e32 v49, v49
	v_exp_f32_e32 v50, v50
	v_exp_f32_e32 v51, v51
	v_mfma_f32_32x32x16_f16 v[16:31], v[132:135], v[112:115], v[16:31]
	v_fma_f32 v52, v52, s8, -v208
	v_fma_f32 v53, v53, s8, -v208
	v_fma_f32 v54, v54, s8, -v208
	v_fma_f32 v55, v55, s8, -v208
	v_exp_f32_e32 v52, v52
	v_exp_f32_e32 v53, v53
	v_exp_f32_e32 v54, v54
	v_exp_f32_e32 v55, v55
	s_mov_b64 s[4:5], 0x780000
	v_lshl_add_u64 v[108:109], v[162:163], 0, s[4:5]
	s_mov_b32 m0, s37
	s_nop 0
	global_load_lds_dwordx4 v[108:109], off
	v_lshl_add_u64 v[226:227], v[108:109], 0, s[58:59]
	s_add_i32 m0, s37, 0x6800
	s_nop 0
	global_load_lds_dwordx4 v[226:227], off
	s_mov_b64 s[4:5], 0x1f00
	s_waitcnt lgkmcnt(0)
	v_lshl_add_u64 v[108:109], v[164:165], 0, s[4:5]
	v_lshl_add_u64 v[108:109], v[108:109], 0, s[62:63]
	s_add_i32 m0, s38, s65
	s_nop 0
	global_load_lds_dwordx4 v[108:109], off nt
	ds_read_b128 v[112:115], v209
	ds_read_b128 v[116:119], v210
	v_mfma_f32_32x32x16_f16 v[0:15], v[128:131], v[104:107], v[0:15]
	v_fma_f32 v56, v56, s8, -v208
	v_fma_f32 v57, v57, s8, -v208
	v_fma_f32 v58, v58, s8, -v208
	v_fma_f32 v59, v59, s8, -v208
	v_exp_f32_e32 v56, v56
	v_exp_f32_e32 v57, v57
	v_exp_f32_e32 v58, v58
	v_exp_f32_e32 v59, v59
	s_cmp_lg_u32 0, -1
	s_cselect_b32 s9, 0, 0
	s_add_i32 s7, s9, s7
	v_lshl_add_u64 v[104:105], v[178:179], 0, s[4:5]
	v_lshl_add_u64 v[104:105], v[104:105], 0, s[62:63]
	s_add_i32 s9, s7, 0x14c00
	s_add_i32 m0, s9, s65
	s_nop 0
	global_load_lds_dwordx4 v[104:105], off nt
	ds_read_b128 v[104:107], v209 offset:2048
	ds_read_b128 v[108:111], v210 offset:2048
	v_mfma_f32_32x32x16_f16 v[16:31], v[128:131], v[152:155], v[16:31]
	v_fma_f32 v60, v60, s8, -v208
	v_fma_f32 v61, v61, s8, -v208
	v_fma_f32 v62, v62, s8, -v208
	v_fma_f32 v63, v63, s8, -v208
	v_exp_f32_e32 v60, v60
	v_exp_f32_e32 v61, v61
	v_exp_f32_e32 v62, v62
	v_exp_f32_e32 v63, v63
	v_lshl_add_u64 v[128:129], v[176:177], 0, s[4:5]
	v_lshl_add_u64 v[128:129], v[128:129], 0, s[62:63]
	s_add_i32 s9, s7, 0x15000
	s_add_i32 m0, s9, s65
	s_nop 0
	global_load_lds_dwordx4 v[128:129], off nt
	v_mfma_f32_32x32x16_f16 v[0:15], v[124:127], v[148:151], v[0:15]
	v_fma_f32 v32, v32, s8, -v208
	v_fma_f32 v33, v33, s8, -v208
	v_fma_f32 v34, v34, s8, -v208
	v_fma_f32 v35, v35, s8, -v208
	v_exp_f32_e32 v32, v32
	v_exp_f32_e32 v33, v33
	v_exp_f32_e32 v34, v34
	v_exp_f32_e32 v35, v35
	v_lshl_add_u64 v[128:129], v[174:175], 0, s[4:5]
	v_lshl_add_u64 v[128:129], v[128:129], 0, s[62:63]
	s_add_i32 s9, s7, 0x15400
	s_add_i32 m0, s9, s65
	s_nop 0
	global_load_lds_dwordx4 v[128:129], off nt
	s_waitcnt lgkmcnt(14)
	v_mfma_f32_32x32x16_f16 v[16:31], v[124:127], v[144:147], v[16:31]
	v_fma_f32 v36, v36, s8, -v208
	v_fma_f32 v37, v37, s8, -v208
	v_fma_f32 v38, v38, s8, -v208
	v_fma_f32 v39, v39, s8, -v208
	v_exp_f32_e32 v36, v36
	v_exp_f32_e32 v37, v37
	v_exp_f32_e32 v38, v38
	v_exp_f32_e32 v39, v39
	s_add_i32 s9, s7, 0x15800
	v_mfma_f32_32x32x16_f16 v[0:15], v[120:123], v[140:143], v[0:15]
	v_fma_f32 v40, v40, s8, -v208
	v_fma_f32 v41, v41, s8, -v208
	v_fma_f32 v42, v42, s8, -v208
	v_fma_f32 v43, v43, s8, -v208
	v_exp_f32_e32 v40, v40
	v_exp_f32_e32 v41, v41
	v_exp_f32_e32 v42, v42
	v_exp_f32_e32 v43, v43
	s_add_i32 s9, s7, 0x15c00
	s_waitcnt lgkmcnt(12)
	v_mfma_f32_32x32x16_f16 v[16:31], v[120:123], v[136:139], v[16:31]
	v_fma_f32 v44, v44, s8, -v208
	v_fma_f32 v45, v45, s8, -v208
	v_fma_f32 v46, v46, s8, -v208
	v_fma_f32 v47, v47, s8, -v208
	v_exp_f32_e32 v44, v44
	v_exp_f32_e32 v45, v45
	v_exp_f32_e32 v46, v46
	v_exp_f32_e32 v47, v47
	s_add_i32 s8, s7, 0x16000
	s_add_i32 s7, s7, 0x16400
	s_waitcnt vmcnt(6) lgkmcnt(0)
	s_barrier
	ds_read_b128 v[80:83], v221
	ds_read_b128 v[64:67], v161
	ds_read_b128 v[84:87], v184
	ds_read_b128 v[68:71], v211
	ds_read_b128 v[88:91], v212
	ds_read_b128 v[72:75], v213
	ds_read_b128 v[92:95], v214
	ds_read_b128 v[76:79], v215
	s_andn2_b64 vcc, exec, s[2:3]
	s_cbranch_vccnz .LBB6_30
	ds_read_b128 v[136:139], v205 offset:49248
	ds_read_b128 v[140:143], v205 offset:49216
	ds_read_b128 v[144:147], v205 offset:49184
	ds_read_b128 v[148:151], v205 offset:49152
	s_waitcnt lgkmcnt(3)
	v_pk_mul_f32 v[14:15], v[14:15], v[138:139]
	s_waitcnt lgkmcnt(2)
	v_pk_mul_f32 v[10:11], v[10:11], v[142:143]
	s_waitcnt lgkmcnt(1)
	v_pk_mul_f32 v[6:7], v[6:7], v[146:147]
	s_waitcnt lgkmcnt(0)
	v_pk_mul_f32 v[2:3], v[2:3], v[150:151]
	v_pk_mul_f32 v[12:13], v[12:13], v[136:137]
	v_pk_mul_f32 v[8:9], v[8:9], v[140:141]
	v_pk_mul_f32 v[4:5], v[4:5], v[144:145]
	v_pk_mul_f32 v[0:1], v[0:1], v[148:149]
	v_pk_mul_f32 v[30:31], v[30:31], v[138:139]
	v_pk_mul_f32 v[26:27], v[26:27], v[142:143]
	v_pk_mul_f32 v[22:23], v[22:23], v[146:147]
	v_pk_mul_f32 v[18:19], v[18:19], v[150:151]
	v_pk_mul_f32 v[28:29], v[28:29], v[136:137]
	v_pk_mul_f32 v[24:25], v[24:25], v[140:141]
	v_pk_mul_f32 v[20:21], v[20:21], v[144:145]
	v_pk_mul_f32 v[16:17], v[16:17], v[148:149]
.LBB6_30:
	ds_read_b64_tr_b16 v[152:153], v207 offset:40960
	ds_read_b64_tr_b16 v[154:155], v207 offset:41472
	v_add_f32_e32 v120, v48, v49
	v_mov_b32_e32 v121, 0x7f7f7f7f
	v_mov_b32_e32 v124, 0x7c7c7c7c
	s_waitcnt lgkmcnt(2)
	v_mfma_scale_f32_32x32x64_f8f6f4 v[80:95], v[112:119], v[96:103], v[80:95], v121, v124 op_sel_hi:[0,0,0]
	v_add_f32_e32 v112, v50, v120
	v_add_f32_e32 v112, v51, v112
	v_add_f32_e32 v112, v52, v112
	v_add_f32_e32 v116, v53, v112
	v_cvt_pk_f16_f32 v132, v48, v49
	v_cvt_pk_f16_f32 v133, v50, v51
	ds_read_b64_tr_b16 v[112:113], v207 offset:45056
	ds_read_b64_tr_b16 v[114:115], v207 offset:45568
	v_add_f32_e32 v48, v54, v116
	v_add_f32_e32 v48, v55, v48
	v_add_f32_e32 v48, v56, v48
	v_add_f32_e32 v48, v57, v48
	v_cvt_pk_f16_f32 v134, v52, v53
	v_cvt_pk_f16_f32 v135, v54, v55
	s_waitcnt lgkmcnt(4)
	v_mfma_scale_f32_32x32x64_f8f6f4 v[64:79], v[104:111], v[96:103], v[64:79], v121, v124 op_sel_hi:[0,0,0]
	ds_read_b64_tr_b16 v[104:105], v207 offset:41984
	ds_read_b64_tr_b16 v[106:107], v207 offset:42496
	v_add_f32_e32 v48, v58, v48
	v_add_f32_e32 v48, v59, v48
	v_add_f32_e32 v48, v60, v48
	v_add_f32_e32 v48, v61, v48
	v_cvt_pk_f16_f32 v128, v56, v57
	v_cvt_pk_f16_f32 v129, v58, v59
	ds_read_b64_tr_b16 v[156:157], v207 offset:46080
	ds_read_b64_tr_b16 v[158:159], v207 offset:46592
	v_add_f32_e32 v48, v62, v48
	v_add_f32_e32 v48, v63, v48
	v_add_f32_e32 v48, v32, v48
	v_add_f32_e32 v48, v33, v48
	v_cvt_pk_f16_f32 v130, v60, v61
	v_cvt_pk_f16_f32 v131, v62, v63
	ds_read_b64_tr_b16 v[148:149], v207 offset:43008
	ds_read_b64_tr_b16 v[150:151], v207 offset:43520
	v_add_f32_e32 v48, v34, v48
	v_add_f32_e32 v48, v35, v48
	v_add_f32_e32 v48, v36, v48
	v_add_f32_e32 v48, v37, v48
	v_cvt_pk_f16_f32 v124, v32, v33
	v_cvt_pk_f16_f32 v125, v34, v35
	ds_read_b64_tr_b16 v[144:145], v207 offset:47104
	ds_read_b64_tr_b16 v[146:147], v207 offset:47616
	v_add_f32_e32 v32, v38, v48
	v_add_f32_e32 v32, v39, v32
	v_add_f32_e32 v32, v40, v32
	v_add_f32_e32 v32, v41, v32
	v_cvt_pk_f16_f32 v126, v36, v37
	v_cvt_pk_f16_f32 v127, v38, v39
	ds_read_b64_tr_b16 v[140:141], v207 offset:44032
	ds_read_b64_tr_b16 v[142:143], v207 offset:44544
	v_add_f32_e32 v32, v42, v32
	v_add_f32_e32 v32, v43, v32
	v_add_f32_e32 v32, v44, v32
	v_add_f32_e32 v32, v45, v32
	v_cvt_pk_f16_f32 v120, v40, v41
	v_cvt_pk_f16_f32 v121, v42, v43
	ds_read_b64_tr_b16 v[136:137], v207 offset:48128
	ds_read_b64_tr_b16 v[138:139], v207 offset:48640
	v_add_f32_e32 v32, v46, v32
	v_add_f32_e32 v32, v47, v32
	v_add_f32_e32 v32, 0, v32
	v_cvt_pk_f16_f32 v122, v44, v45
	v_cvt_pk_f16_f32 v123, v46, v47
	s_nop 1
	s_nop 0
	v_add_f32_e32 v164, v180, v32
	v_max_f32_e32 v108, v81, v81
	v_max_f32_e32 v109, v80, v80
	v_max_f32_e32 v108, v109, v108
	v_max3_f32 v109, v82, v83, v65
	v_max3_f32 v108, v108, v64, v66
	v_max3_f32 v108, v108, v67, v84
	v_max3_f32 v109, v109, v86, v87
	v_max3_f32 v108, v108, v85, v68
	v_max3_f32 v109, v109, v70, v71
	v_max3_f32 v108, v108, v69, v88
	v_max3_f32 v109, v109, v90, v91
	v_max3_f32 v108, v108, v89, v72
	v_max3_f32 v109, v109, v74, v75
	v_max3_f32 v108, v108, v73, v92
	v_max3_f32 v109, v109, v94, v95
	v_max3_f32 v108, v108, v93, v76
	v_max3_f32 v109, v109, v78, v79
	v_max3_f32 v108, v108, v77, v109
	v_mov_b32_e32 v109, v108
	s_nop 1
	v_permlane32_swap_b32_e32 v108, v109
	v_max_f32_e32 v109, v109, v109
	v_max_f32_e32 v108, v108, v108
	v_max_f32_e32 v108, v108, v109
	s_mov_b32 s7, 0x3fb8aa3b
	v_fma_f32 v108, v108, s7, -v208
	s_mov_b32 s2, 0x41000000
	v_cmp_lt_f32_e32 vcc, s2, v108
	s_cmp_lg_u64 vcc, 0
	s_cselect_b64 s[2:3], -1, 0
	s_cbranch_vccnz .LBB6_42
.LBB6_31:
	s_waitcnt lgkmcnt(14)
	v_mfma_f32_32x32x16_f16 v[0:15], v[132:135], v[152:155], v[0:15]
	v_fma_f32 v80, v80, s7, -v208
	v_fma_f32 v81, v81, s7, -v208
	v_fma_f32 v82, v82, s7, -v208
	v_fma_f32 v83, v83, s7, -v208
	v_exp_f32_e32 v80, v80
	v_exp_f32_e32 v81, v81
	v_exp_f32_e32 v82, v82
	v_exp_f32_e32 v83, v83
	v_mfma_f32_32x32x16_f16 v[16:31], v[132:135], v[112:115], v[16:31]
	v_fma_f32 v84, v84, s7, -v208
	v_fma_f32 v85, v85, s7, -v208
	v_fma_f32 v86, v86, s7, -v208
	v_fma_f32 v87, v87, s7, -v208
	v_exp_f32_e32 v84, v84
	v_exp_f32_e32 v85, v85
	v_exp_f32_e32 v86, v86
	v_exp_f32_e32 v87, v87
	s_mov_b64 s[4:5], 0x7c0000
	s_cmp_lg_u32 0, -1
	v_lshl_add_u64 v[108:109], v[162:163], 0, s[4:5]
	s_cselect_b32 s4, 0, 0
	s_add_i32 s4, s4, s36
	s_add_i32 s4, s4, 0x8000
	s_mov_b32 m0, s4
	s_nop 0
	global_load_lds_dwordx4 v[108:109], off
	v_lshl_add_u64 v[226:227], v[108:109], 0, s[58:59]
	s_add_i32 m0, s4, 0x6800
	s_nop 0
	global_load_lds_dwordx4 v[226:227], off
	ds_read_b128 v[112:115], v209 offset:8192
	ds_read_b128 v[116:119], v210 offset:8192
	v_mfma_f32_32x32x16_f16 v[0:15], v[128:131], v[104:107], v[0:15]
	v_fma_f32 v88, v88, s7, -v208
	v_fma_f32 v89, v89, s7, -v208
	v_fma_f32 v90, v90, s7, -v208
	v_fma_f32 v91, v91, s7, -v208
	v_exp_f32_e32 v88, v88
	v_exp_f32_e32 v89, v89
	v_exp_f32_e32 v90, v90
	v_exp_f32_e32 v91, v91
	ds_read_b128 v[104:107], v209 offset:10240
	ds_read_b128 v[108:111], v210 offset:10240
	v_mfma_f32_32x32x16_f16 v[16:31], v[128:131], v[156:159], v[16:31]
	v_fma_f32 v92, v92, s7, -v208
	v_fma_f32 v93, v93, s7, -v208
	v_fma_f32 v94, v94, s7, -v208
	v_fma_f32 v95, v95, s7, -v208
	v_exp_f32_e32 v92, v92
	v_exp_f32_e32 v93, v93
	v_exp_f32_e32 v94, v94
	v_exp_f32_e32 v95, v95
	v_mfma_f32_32x32x16_f16 v[0:15], v[124:127], v[148:151], v[0:15]
	v_fma_f32 v64, v64, s7, -v208
	v_fma_f32 v65, v65, s7, -v208
	v_fma_f32 v66, v66, s7, -v208
	v_fma_f32 v67, v67, s7, -v208
	v_exp_f32_e32 v64, v64
	v_exp_f32_e32 v65, v65
	v_exp_f32_e32 v66, v66
	v_exp_f32_e32 v67, v67
	s_waitcnt lgkmcnt(14)
	v_mfma_f32_32x32x16_f16 v[16:31], v[124:127], v[144:147], v[16:31]
	v_fma_f32 v68, v68, s7, -v208
	v_fma_f32 v69, v69, s7, -v208
	v_fma_f32 v70, v70, s7, -v208
	v_fma_f32 v71, v71, s7, -v208
	v_exp_f32_e32 v68, v68
	v_exp_f32_e32 v69, v69
	v_exp_f32_e32 v70, v70
	v_exp_f32_e32 v71, v71
	v_mfma_f32_32x32x16_f16 v[0:15], v[120:123], v[140:143], v[0:15]
	v_fma_f32 v72, v72, s7, -v208
	v_fma_f32 v73, v73, s7, -v208
	v_fma_f32 v74, v74, s7, -v208
	v_fma_f32 v75, v75, s7, -v208
	v_exp_f32_e32 v72, v72
	v_exp_f32_e32 v73, v73
	v_exp_f32_e32 v74, v74
	v_exp_f32_e32 v75, v75
	s_waitcnt lgkmcnt(12)
	v_mfma_f32_32x32x16_f16 v[16:31], v[120:123], v[136:139], v[16:31]
	v_fma_f32 v76, v76, s7, -v208
	v_fma_f32 v77, v77, s7, -v208
	v_fma_f32 v78, v78, s7, -v208
	v_fma_f32 v79, v79, s7, -v208
	v_exp_f32_e32 v76, v76
	v_exp_f32_e32 v77, v77
	v_exp_f32_e32 v78, v78
	v_exp_f32_e32 v79, v79
	s_waitcnt vmcnt(0) lgkmcnt(0)
	s_barrier
	ds_read_b128 v[48:51], v221 offset:32768
	ds_read_b128 v[32:35], v161 offset:32768
	ds_read_b128 v[52:55], v184 offset:32768
	ds_read_b128 v[36:39], v211 offset:32768
	ds_read_b128 v[56:59], v212 offset:32768
	ds_read_b128 v[40:43], v213 offset:32768
	ds_read_b128 v[60:63], v214 offset:32768
	ds_read_b128 v[44:47], v215 offset:32768
	s_andn2_b64 vcc, exec, s[2:3]
	s_cbranch_vccnz .LBB6_33
	ds_read_b128 v[136:139], v205 offset:49248
	ds_read_b128 v[140:143], v205 offset:49216
	ds_read_b128 v[144:147], v205 offset:49184
	ds_read_b128 v[148:151], v205 offset:49152
	s_waitcnt lgkmcnt(3)
	v_pk_mul_f32 v[14:15], v[14:15], v[138:139]
	s_waitcnt lgkmcnt(2)
	v_pk_mul_f32 v[10:11], v[10:11], v[142:143]
	s_waitcnt lgkmcnt(1)
	v_pk_mul_f32 v[6:7], v[6:7], v[146:147]
	s_waitcnt lgkmcnt(0)
	v_pk_mul_f32 v[2:3], v[2:3], v[150:151]
	v_pk_mul_f32 v[12:13], v[12:13], v[136:137]
	v_pk_mul_f32 v[8:9], v[8:9], v[140:141]
	v_pk_mul_f32 v[4:5], v[4:5], v[144:145]
	v_pk_mul_f32 v[0:1], v[0:1], v[148:149]
	v_pk_mul_f32 v[30:31], v[30:31], v[138:139]
	v_pk_mul_f32 v[26:27], v[26:27], v[142:143]
	v_pk_mul_f32 v[22:23], v[22:23], v[146:147]
	v_pk_mul_f32 v[18:19], v[18:19], v[150:151]
	v_pk_mul_f32 v[28:29], v[28:29], v[136:137]
	v_pk_mul_f32 v[24:25], v[24:25], v[140:141]
	v_pk_mul_f32 v[20:21], v[20:21], v[144:145]
	v_pk_mul_f32 v[16:17], v[16:17], v[148:149]
.LBB6_33:
	ds_read_b64_tr_b16 v[136:137], v207 offset:24576
	ds_read_b64_tr_b16 v[138:139], v207 offset:25088
	v_add_f32_e32 v120, v80, v81
	v_mov_b32_e32 v121, 0x7f7f7f7f
	v_mov_b32_e32 v124, 0x7c7c7c7c
	s_waitcnt lgkmcnt(2)
	v_mfma_scale_f32_32x32x64_f8f6f4 v[48:63], v[112:119], v[96:103], v[48:63], v121, v124 op_sel_hi:[0,0,0]
	v_add_f32_e32 v112, v82, v120
	v_add_f32_e32 v112, v83, v112
	v_add_f32_e32 v112, v84, v112
	v_add_f32_e32 v116, v85, v112
	v_cvt_pk_f16_f32 v132, v80, v81
	v_cvt_pk_f16_f32 v133, v82, v83
	ds_read_b64_tr_b16 v[112:113], v207 offset:28672
	ds_read_b64_tr_b16 v[114:115], v207 offset:29184
	v_add_f32_e32 v80, v86, v116
	v_add_f32_e32 v80, v87, v80
	v_add_f32_e32 v80, v88, v80
	v_add_f32_e32 v80, v89, v80
	v_cvt_pk_f16_f32 v134, v84, v85
	v_cvt_pk_f16_f32 v135, v86, v87
	s_waitcnt lgkmcnt(4)
	v_mfma_scale_f32_32x32x64_f8f6f4 v[32:47], v[104:111], v[96:103], v[32:47], v121, v124 op_sel_hi:[0,0,0]
	ds_read_b64_tr_b16 v[96:97], v207 offset:25600
	ds_read_b64_tr_b16 v[98:99], v207 offset:26112
	v_add_f32_e32 v80, v90, v80
	v_add_f32_e32 v80, v91, v80
	v_add_f32_e32 v80, v92, v80
	v_add_f32_e32 v80, v93, v80
	v_cvt_pk_f16_f32 v128, v88, v89
	v_cvt_pk_f16_f32 v129, v90, v91
	ds_read_b64_tr_b16 v[88:89], v207 offset:29696
	ds_read_b64_tr_b16 v[90:91], v207 offset:30208
	v_add_f32_e32 v80, v94, v80
	v_add_f32_e32 v80, v95, v80
	v_add_f32_e32 v80, v64, v80
	v_add_f32_e32 v80, v65, v80
	v_cvt_pk_f16_f32 v130, v92, v93
	v_cvt_pk_f16_f32 v131, v94, v95
	ds_read_b64_tr_b16 v[84:85], v207 offset:26624
	ds_read_b64_tr_b16 v[86:87], v207 offset:27136
	v_add_f32_e32 v80, v66, v80
	v_add_f32_e32 v80, v67, v80
	v_add_f32_e32 v80, v68, v80
	v_add_f32_e32 v92, v69, v80
	v_cvt_pk_f16_f32 v124, v64, v65
	v_cvt_pk_f16_f32 v125, v66, v67
	ds_read_b64_tr_b16 v[80:81], v207 offset:30720
	ds_read_b64_tr_b16 v[82:83], v207 offset:31232
	v_add_f32_e32 v64, v70, v92
	v_add_f32_e32 v64, v71, v64
	v_add_f32_e32 v64, v72, v64
	v_add_f32_e32 v64, v73, v64
	v_cvt_pk_f16_f32 v126, v68, v69
	v_cvt_pk_f16_f32 v127, v70, v71
	ds_read_b64_tr_b16 v[68:69], v207 offset:27648
	ds_read_b64_tr_b16 v[70:71], v207 offset:28160
	v_add_f32_e32 v64, v74, v64
	v_add_f32_e32 v64, v75, v64
	v_add_f32_e32 v64, v76, v64
	v_add_f32_e32 v92, v77, v64
	v_cvt_pk_f16_f32 v120, v72, v73
	v_cvt_pk_f16_f32 v121, v74, v75
	ds_read_b64_tr_b16 v[64:65], v207 offset:31744
	ds_read_b64_tr_b16 v[66:67], v207 offset:32256
	v_add_f32_e32 v72, v78, v92
	v_add_f32_e32 v72, v79, v72
	v_add_f32_e32 v72, 0, v72
	v_cvt_pk_f16_f32 v122, v76, v77
	v_cvt_pk_f16_f32 v123, v78, v79
	s_nop 1
	s_mov_b32 s2, 0x41000000
	v_max_f32_e32 v73, v49, v49
	v_max_f32_e32 v74, v48, v48
	v_max_f32_e32 v73, v74, v73
	v_max3_f32 v74, v50, v51, v33
	v_max3_f32 v73, v73, v32, v34
	v_max3_f32 v73, v73, v35, v52
	v_max3_f32 v74, v74, v54, v55
	v_max3_f32 v73, v73, v53, v36
	v_max3_f32 v74, v74, v38, v39
	v_max3_f32 v73, v73, v37, v56
	v_max3_f32 v74, v74, v58, v59
	v_max3_f32 v73, v73, v57, v40
	v_max3_f32 v74, v74, v42, v43
	v_max3_f32 v73, v73, v41, v60
	v_max3_f32 v74, v74, v62, v63
	v_max3_f32 v73, v73, v61, v44
	v_max3_f32 v74, v74, v46, v47
	v_max3_f32 v73, v73, v45, v74
	v_mov_b32_e32 v74, v73
	s_nop 1
	v_permlane32_swap_b32_e32 v73, v74
	v_max_f32_e32 v74, v74, v74
	v_max_f32_e32 v73, v73, v73
	v_max_f32_e32 v73, v73, v74
	v_fma_f32 v73, v73, s7, -v208
	v_cmp_lt_f32_e32 vcc, s2, v73
	s_cmp_lg_u64 vcc, 0
	v_add_f32_e32 v72, v164, v72
	s_cselect_b64 s[2:3], -1, 0
	s_cbranch_vccnz .LBB6_45
